# converter throttle s_sleep 55 per k-block
# baseline (speedup 1.0000x reference)
; DI s16x4 tr16(const LAS unsigned char* p) { return __builtin_bit_cast(s16x4, __builtin_amdgcn_ds_read_tr16_b64_v4i16((LAS v4i16_t*)p)); }
; #define LDS_WAIT() asm volatile("s_waitcnt lgkmcnt(0)" ::: "memory")
; #define P0S_LOAD(dst, krow0) do { _Pragma("unroll") for (int i = 0; i < 16; ++i) dst[i] = *(const f32x4*)(wp + (size_t)((krow0) + 2 * i) * ld); } while (0)
; #define P0S_PUT(src, r0) do { _Pragma("unroll") for (int i = 0; i < 16; ++i) { \
;         u32x2 pk; pk.x = cvtpk(src[i][0], src[i][1]) + 0x02800280u; pk.y = cvtpk(src[i][2], src[i][3]) + 0x02800280u;        \
;         *(LAS u32x2*)(img + wb[i & 7] + ((r0) / 16 + (i >> 3)) * 4096) = pk; } } while (0)
; #define P0S_F8(lo, hi) pk4_fp8m(__uint_as_float((lo) << 16), __uint_as_float((lo) & 0xffff0000u), __uint_as_float((hi) << 16), __uint_as_float((hi) & 0xffff0000u))
; template <int MODE>
; DI void p0_strip_fp8(const float* W, int ld, unsigned char* WT, int K, int n0, LAS unsigned char* img, int lane) {
;     ...
;     P0S_LOAD(va, 0);
; #pragma unroll 1
;     for (int kb = 0; kb < 32; ++kb) {
;         P0S_LOAD(vb, 64 * kb + 32);
;         P0S_PUT(va, 0);
;         if (kb < 31) P0S_LOAD(va, 64 * kb + 64);
;         P0S_PUT(vb, 32);
;         LDS_WAIT();
; #pragma unroll 2
;         for (int nb = 0; nb < 8; ++nb) {
;             const s16x4 t0 = tr16(img + rb[0] + 32 * (nb ^ cx[0])), t1 = tr16(img + rb[1] + 32 * (nb ^ cx[1])), t2 = tr16(img + rb[2] + 32 * (nb ^ cx[2])), t3 = tr16(img + rb[3] + 32 * (nb ^ cx[3]));
;             const u32x2 f0 = __builtin_bit_cast(u32x2, t0), f1 = __builtin_bit_cast(u32x2, t1), f2 = __builtin_bit_cast(u32x2, t2), f3 = __builtin_bit_cast(u32x2, t3);
;             u32x4 o; o.x = P0S_F8(f0.x, f0.y); o.y = P0S_F8(f1.x, f1.y); o.z = P0S_F8(f2.x, f2.y); o.w = P0S_F8(f3.x, f3.y);
;             *(u32x4*)(WT + (size_t)(unsigned)orow[nb] + 64 * kb) = o; }
;         LDS_WAIT();
;     }
.LBB0_281:
	v_xor_b32_e32 v82, s2, v150
	v_xor_b32_e32 v83, s2, v151
	s_cmp_eq_u32 s2, 1
	v_lshlrev_b32_e32 v82, 5, v82
	v_lshlrev_b32_e32 v83, 5, v83
	s_cselect_b64 vcc, -1, 0
	s_cmp_eq_u32 s2, 2
	v_cndmask_b32_e32 v84, v2, v1, vcc
	v_add_u32_e32 v85, v152, v82
	v_add_u32_e32 v86, v153, v82
	v_add_u32_e32 v87, v152, v83
	v_add_u32_e32 v88, v153, v83
	s_cselect_b64 vcc, -1, 0
	s_cmp_eq_u32 s2, 3
	v_cndmask_b32_e32 v90, v84, v4, vcc
	ds_read_b64_tr_b16 v[82:83], v85
	ds_read_b64_tr_b16 v[84:85], v86 offset:1024
	ds_read_b64_tr_b16 v[86:87], v87 offset:2048
	ds_read_b64_tr_b16 v[88:89], v88 offset:3072
	s_cselect_b64 vcc, -1, 0
	s_cmp_eq_u32 s2, 4
	v_cndmask_b32_e32 v90, v90, v3, vcc
	s_cselect_b64 vcc, -1, 0
	s_cmp_eq_u32 s2, 5
	v_cndmask_b32_e32 v90, v90, v6, vcc
	s_cselect_b64 vcc, -1, 0
	s_cmp_eq_u32 s2, 6
	v_cndmask_b32_e32 v90, v90, v5, vcc
	s_cselect_b64 vcc, -1, 0
	s_cmp_eq_u32 s2, 7
	v_cndmask_b32_e32 v90, v90, v8, vcc
	s_cselect_b64 vcc, -1, 0
	s_add_i32 s63, s2, 1
	s_waitcnt lgkmcnt(3)
	v_lshlrev_b32_e32 v91, 16, v82
	v_and_b32_e32 v82, 0xffff0000, v82
	v_lshlrev_b32_e32 v92, 16, v83
	v_and_b32_e32 v83, 0xffff0000, v83
	s_waitcnt lgkmcnt(2)
	v_lshlrev_b32_e32 v93, 16, v84
	v_and_b32_e32 v84, 0xffff0000, v84
	v_lshlrev_b32_e32 v94, 16, v85
	v_and_b32_e32 v85, 0xffff0000, v85
	s_waitcnt lgkmcnt(1)
	v_lshlrev_b32_e32 v95, 16, v86
	v_and_b32_e32 v86, 0xffff0000, v86
	v_lshlrev_b32_e32 v96, 16, v87
	v_and_b32_e32 v87, 0xffff0000, v87
	s_waitcnt lgkmcnt(0)
	v_lshlrev_b32_e32 v97, 16, v88
	v_and_b32_e32 v88, 0xffff0000, v88
	v_lshlrev_b32_e32 v98, 16, v89
	v_and_b32_e32 v89, 0xffff0000, v89
	v_xor_b32_e32 v99, s63, v150
	v_xor_b32_e32 v100, s63, v151
	v_mov_b32_e32 v74, 0
	v_mov_b32_e32 v75, 0
	v_mov_b32_e32 v76, 0
	v_mov_b32_e32 v77, 0
	v_med3_f32 v91, v91, s52, v163
	v_med3_f32 v82, v82, s52, v163
	v_med3_f32 v101, v83, s52, v163
	v_med3_f32 v83, v93, s52, v163
	v_med3_f32 v84, v84, s52, v163
	v_med3_f32 v93, v94, s52, v163
	v_med3_f32 v94, v85, s52, v163
	v_med3_f32 v85, v95, s52, v163
	v_med3_f32 v86, v86, s52, v163
	v_med3_f32 v95, v96, s52, v163
	v_med3_f32 v96, v87, s52, v163
	v_med3_f32 v87, v97, s52, v163
	v_med3_f32 v88, v88, s52, v163
	v_med3_f32 v97, v98, s52, v163
	v_med3_f32 v98, v89, s52, v163
	v_lshlrev_b32_e32 v89, 5, v99
	v_lshlrev_b32_e32 v99, 5, v100
	v_cvt_pk_fp8_f32 v74, v91, v82
	v_cvt_pk_fp8_f32 v75, v83, v84
	v_cvt_pk_fp8_f32 v76, v85, v86
	v_cvt_pk_fp8_f32 v77, v87, v88
	v_add_u32_e32 v82, v152, v89
	v_add_u32_e32 v84, v153, v89
	v_add_u32_e32 v86, v152, v99
	v_add_u32_e32 v88, v153, v99
	ds_read_b64_tr_b16 v[82:83], v82
	ds_read_b64_tr_b16 v[84:85], v84 offset:1024
	ds_read_b64_tr_b16 v[86:87], v86 offset:2048
	ds_read_b64_tr_b16 v[88:89], v88 offset:3072
	v_med3_f32 v92, v92, s52, v163
	s_cmp_eq_u32 s63, 1
	v_cvt_pk_fp8_f32 v74, v92, v101 op_sel:[0,0,1]
	v_cvt_pk_fp8_f32 v75, v93, v94 op_sel:[0,0,1]
	v_cvt_pk_fp8_f32 v76, v95, v96 op_sel:[0,0,1]
	v_cvt_pk_fp8_f32 v77, v97, v98 op_sel:[0,0,1]
	s_waitcnt lgkmcnt(3)
	v_lshlrev_b32_e32 v92, 16, v82
	v_and_b32_e32 v82, 0xffff0000, v82
	s_waitcnt lgkmcnt(2)
	v_lshlrev_b32_e32 v94, 16, v84
	v_and_b32_e32 v84, 0xffff0000, v84
	s_waitcnt lgkmcnt(1)
	v_lshlrev_b32_e32 v96, 16, v86
	v_and_b32_e32 v86, 0xffff0000, v86
	s_waitcnt lgkmcnt(0)
	v_lshlrev_b32_e32 v98, 16, v88
	v_and_b32_e32 v88, 0xffff0000, v88
	v_mov_b32_e32 v78, 0
	v_mov_b32_e32 v79, 0
	v_mov_b32_e32 v80, 0
	v_mov_b32_e32 v81, 0
	v_cndmask_b32_e32 v90, v90, v7, vcc
	s_cselect_b64 vcc, -1, 0
	s_cmp_eq_u32 s63, 2
	v_med3_f32 v92, v92, s52, v163
	v_med3_f32 v82, v82, s52, v163
	v_med3_f32 v94, v94, s52, v163
	v_med3_f32 v84, v84, s52, v163
	v_med3_f32 v96, v96, s52, v163
	v_med3_f32 v86, v86, s52, v163
	v_med3_f32 v98, v98, s52, v163
	v_med3_f32 v88, v88, s52, v163
	v_cndmask_b32_e32 v100, v2, v1, vcc
	s_cselect_b64 vcc, -1, 0
	s_cmp_eq_u32 s63, 3
	v_cvt_pk_fp8_f32 v78, v92, v82
	v_cvt_pk_fp8_f32 v79, v94, v84
	v_cvt_pk_fp8_f32 v80, v96, v86
	v_cvt_pk_fp8_f32 v81, v98, v88
	v_cndmask_b32_e32 v91, v100, v4, vcc
	s_cselect_b64 vcc, -1, 0
	s_cmp_eq_u32 s63, 4
	v_cndmask_b32_e32 v91, v91, v3, vcc
	s_cselect_b64 vcc, -1, 0
	s_cmp_eq_u32 s63, 5
	v_lshlrev_b32_e32 v93, 16, v83
	v_and_b32_e32 v83, 0xffff0000, v83
	v_lshlrev_b32_e32 v95, 16, v85
	v_and_b32_e32 v85, 0xffff0000, v85
	v_lshlrev_b32_e32 v97, 16, v87
	v_and_b32_e32 v87, 0xffff0000, v87
	v_lshlrev_b32_e32 v99, 16, v89
	v_and_b32_e32 v89, 0xffff0000, v89
	v_cndmask_b32_e32 v91, v91, v6, vcc
	s_cselect_b64 vcc, -1, 0
	s_cmp_eq_u32 s63, 6
	v_med3_f32 v93, v93, s52, v163
	v_med3_f32 v83, v83, s52, v163
	v_med3_f32 v95, v95, s52, v163
	v_med3_f32 v85, v85, s52, v163
	v_med3_f32 v97, v97, s52, v163
	v_med3_f32 v87, v87, s52, v163
	v_med3_f32 v99, v99, s52, v163
	v_med3_f32 v89, v89, s52, v163
	v_cndmask_b32_e32 v91, v91, v5, vcc
	s_cselect_b64 vcc, -1, 0
	s_cmp_eq_u32 s63, 7
	v_cvt_pk_fp8_f32 v78, v93, v83 op_sel:[0,0,1]
	v_cvt_pk_fp8_f32 v79, v95, v85 op_sel:[0,0,1]
	v_cvt_pk_fp8_f32 v80, v97, v87 op_sel:[0,0,1]
	v_cvt_pk_fp8_f32 v81, v99, v89 op_sel:[0,0,1]
	v_cndmask_b32_e32 v91, v91, v8, vcc
	s_cselect_b64 vcc, -1, 0
	s_add_i32 s2, s2, 2
	s_cmp_eq_u32 s2, 8
	v_cndmask_b32_e32 v91, v91, v7, vcc
	global_store_dwordx4 v90, v[74:77], s[6:7]
	global_store_dwordx4 v91, v[78:81], s[6:7]
	s_cbranch_scc0 .LBB0_281
	s_sleep 55
	s_waitcnt lgkmcnt(0)
	s_add_i32 s62, s62, 1
	s_cmp_eq_u32 s62, 32
	s_cbranch_scc0 .LBB0_278
	s_mov_b64 s[0:1], 0

; DI s16x4 tr16(const LAS unsigned char* p) { return __builtin_bit_cast(s16x4, __builtin_amdgcn_ds_read_tr16_b64_v4i16((LAS v4i16_t*)p)); }
; #define LDS_WAIT() asm volatile("s_waitcnt lgkmcnt(0)" ::: "memory")
; #define P0S_LOAD(dst, krow0) do { _Pragma("unroll") for (int i = 0; i < 16; ++i) dst[i] = *(const f32x4*)(wp + (size_t)((krow0) + 2 * i) * ld); } while (0)
; #define P0S_PUT(src, r0) do { _Pragma("unroll") for (int i = 0; i < 16; ++i) { \
;         u32x2 pk; pk.x = cvtpk(src[i][0], src[i][1]) + 0x02800280u; pk.y = cvtpk(src[i][2], src[i][3]) + 0x02800280u;        \
;         *(LAS u32x2*)(img + wb[i & 7] + ((r0) / 16 + (i >> 3)) * 4096) = pk; } } while (0)
; #define P0S_F8(lo, hi) pk4_fp8m(__uint_as_float((lo) << 16), __uint_as_float((lo) & 0xffff0000u), __uint_as_float((hi) << 16), __uint_as_float((hi) & 0xffff0000u))
; template <int MODE>
; DI void p0_strip_fp8(const float* W, int ld, unsigned char* WT, int K, int n0, LAS unsigned char* img, int lane) {
;     ...
;     P0S_LOAD(va, 0);
; #pragma unroll 1
;     for (int kb = 0; kb < 32; ++kb) {
;         P0S_LOAD(vb, 64 * kb + 32);
;         P0S_PUT(va, 0);
;         if (kb < 31) P0S_LOAD(va, 64 * kb + 64);
;         P0S_PUT(vb, 32);
;         LDS_WAIT();
; #pragma unroll 2
;         for (int nb = 0; nb < 8; ++nb) {
;             const s16x4 t0 = tr16(img + rb[0] + 32 * (nb ^ cx[0])), t1 = tr16(img + rb[1] + 32 * (nb ^ cx[1])), t2 = tr16(img + rb[2] + 32 * (nb ^ cx[2])), t3 = tr16(img + rb[3] + 32 * (nb ^ cx[3]));
;             const u32x2 f0 = __builtin_bit_cast(u32x2, t0), f1 = __builtin_bit_cast(u32x2, t1), f2 = __builtin_bit_cast(u32x2, t2), f3 = __builtin_bit_cast(u32x2, t3);
;             u32x4 o; o.x = P0S_F8(f0.x, f0.y); o.y = P0S_F8(f1.x, f1.y); o.z = P0S_F8(f2.x, f2.y); o.w = P0S_F8(f3.x, f3.y);
;             *(u32x4*)(WT + (size_t)(unsigned)orow[nb] + 64 * kb) = o; }
;         LDS_WAIT();
;     }
.LBB0_289:
	v_xor_b32_e32 v82, s2, v150
	v_xor_b32_e32 v83, s2, v151
	s_cmp_eq_u32 s2, 1
	v_lshlrev_b32_e32 v82, 5, v82
	v_lshlrev_b32_e32 v83, 5, v83
	s_cselect_b64 vcc, -1, 0
	s_cmp_eq_u32 s2, 2
	v_cndmask_b32_e32 v84, v2, v1, vcc
	v_add_u32_e32 v85, v152, v82
	v_add_u32_e32 v86, v153, v82
	v_add_u32_e32 v87, v152, v83
	v_add_u32_e32 v88, v153, v83
	s_cselect_b64 vcc, -1, 0
	s_cmp_eq_u32 s2, 3
	v_cndmask_b32_e32 v90, v84, v4, vcc
	ds_read_b64_tr_b16 v[82:83], v85
	ds_read_b64_tr_b16 v[84:85], v86 offset:1024
	ds_read_b64_tr_b16 v[86:87], v87 offset:2048
	ds_read_b64_tr_b16 v[88:89], v88 offset:3072
	s_cselect_b64 vcc, -1, 0
	s_cmp_eq_u32 s2, 4
	v_cndmask_b32_e32 v90, v90, v3, vcc
	s_cselect_b64 vcc, -1, 0
	s_cmp_eq_u32 s2, 5
	v_cndmask_b32_e32 v90, v90, v6, vcc
	s_cselect_b64 vcc, -1, 0
	s_cmp_eq_u32 s2, 6
	v_cndmask_b32_e32 v90, v90, v5, vcc
	s_cselect_b64 vcc, -1, 0
	s_cmp_eq_u32 s2, 7
	v_cndmask_b32_e32 v90, v90, v8, vcc
	s_cselect_b64 vcc, -1, 0
	s_add_i32 s62, s2, 1
	s_waitcnt lgkmcnt(3)
	v_lshlrev_b32_e32 v91, 16, v82
	v_and_b32_e32 v82, 0xffff0000, v82
	v_lshlrev_b32_e32 v92, 16, v83
	v_and_b32_e32 v83, 0xffff0000, v83
	s_waitcnt lgkmcnt(2)
	v_lshlrev_b32_e32 v93, 16, v84
	v_and_b32_e32 v84, 0xffff0000, v84
	v_lshlrev_b32_e32 v94, 16, v85
	v_and_b32_e32 v85, 0xffff0000, v85
	s_waitcnt lgkmcnt(1)
	v_lshlrev_b32_e32 v95, 16, v86
	v_and_b32_e32 v86, 0xffff0000, v86
	v_lshlrev_b32_e32 v96, 16, v87
	v_and_b32_e32 v87, 0xffff0000, v87
	s_waitcnt lgkmcnt(0)
	v_lshlrev_b32_e32 v97, 16, v88
	v_and_b32_e32 v88, 0xffff0000, v88
	v_lshlrev_b32_e32 v98, 16, v89
	v_and_b32_e32 v89, 0xffff0000, v89
	v_xor_b32_e32 v99, s62, v150
	v_xor_b32_e32 v100, s62, v151
	v_mov_b32_e32 v74, 0
	v_mov_b32_e32 v75, 0
	v_mov_b32_e32 v76, 0
	v_mov_b32_e32 v77, 0
	v_med3_f32 v91, v91, s52, v163
	v_med3_f32 v82, v82, s52, v163
	v_med3_f32 v101, v83, s52, v163
	v_med3_f32 v83, v93, s52, v163
	v_med3_f32 v84, v84, s52, v163
	v_med3_f32 v93, v94, s52, v163
	v_med3_f32 v94, v85, s52, v163
	v_med3_f32 v85, v95, s52, v163
	v_med3_f32 v86, v86, s52, v163
	v_med3_f32 v95, v96, s52, v163
	v_med3_f32 v96, v87, s52, v163
	v_med3_f32 v87, v97, s52, v163
	v_med3_f32 v88, v88, s52, v163
	v_med3_f32 v97, v98, s52, v163
	v_med3_f32 v98, v89, s52, v163
	v_lshlrev_b32_e32 v89, 5, v99
	v_lshlrev_b32_e32 v99, 5, v100
	v_cvt_pk_fp8_f32 v74, v91, v82
	v_cvt_pk_fp8_f32 v75, v83, v84
	v_cvt_pk_fp8_f32 v76, v85, v86
	v_cvt_pk_fp8_f32 v77, v87, v88
	v_add_u32_e32 v82, v152, v89
	v_add_u32_e32 v84, v153, v89
	v_add_u32_e32 v86, v152, v99
	v_add_u32_e32 v88, v153, v99
	ds_read_b64_tr_b16 v[82:83], v82
	ds_read_b64_tr_b16 v[84:85], v84 offset:1024
	ds_read_b64_tr_b16 v[86:87], v86 offset:2048
	ds_read_b64_tr_b16 v[88:89], v88 offset:3072
	v_med3_f32 v92, v92, s52, v163
	s_cmp_eq_u32 s62, 1
	v_cvt_pk_fp8_f32 v74, v92, v101 op_sel:[0,0,1]
	v_cvt_pk_fp8_f32 v75, v93, v94 op_sel:[0,0,1]
	v_cvt_pk_fp8_f32 v76, v95, v96 op_sel:[0,0,1]
	v_cvt_pk_fp8_f32 v77, v97, v98 op_sel:[0,0,1]
	s_waitcnt lgkmcnt(3)
	v_lshlrev_b32_e32 v92, 16, v82
	v_and_b32_e32 v82, 0xffff0000, v82
	s_waitcnt lgkmcnt(2)
	v_lshlrev_b32_e32 v94, 16, v84
	v_and_b32_e32 v84, 0xffff0000, v84
	s_waitcnt lgkmcnt(1)
	v_lshlrev_b32_e32 v96, 16, v86
	v_and_b32_e32 v86, 0xffff0000, v86
	s_waitcnt lgkmcnt(0)
	v_lshlrev_b32_e32 v98, 16, v88
	v_and_b32_e32 v88, 0xffff0000, v88
	v_mov_b32_e32 v78, 0
	v_mov_b32_e32 v79, 0
	v_mov_b32_e32 v80, 0
	v_mov_b32_e32 v81, 0
	v_cndmask_b32_e32 v90, v90, v7, vcc
	s_cselect_b64 vcc, -1, 0
	s_cmp_eq_u32 s62, 2
	v_med3_f32 v92, v92, s52, v163
	v_med3_f32 v82, v82, s52, v163
	v_med3_f32 v94, v94, s52, v163
	v_med3_f32 v84, v84, s52, v163
	v_med3_f32 v96, v96, s52, v163
	v_med3_f32 v86, v86, s52, v163
	v_med3_f32 v98, v98, s52, v163
	v_med3_f32 v88, v88, s52, v163
	v_cndmask_b32_e32 v100, v2, v1, vcc
	s_cselect_b64 vcc, -1, 0
	s_cmp_eq_u32 s62, 3
	v_cvt_pk_fp8_f32 v78, v92, v82
	v_cvt_pk_fp8_f32 v79, v94, v84
	v_cvt_pk_fp8_f32 v80, v96, v86
	v_cvt_pk_fp8_f32 v81, v98, v88
	v_cndmask_b32_e32 v91, v100, v4, vcc
	s_cselect_b64 vcc, -1, 0
	s_cmp_eq_u32 s62, 4
	v_cndmask_b32_e32 v91, v91, v3, vcc
	s_cselect_b64 vcc, -1, 0
	s_cmp_eq_u32 s62, 5
	v_lshlrev_b32_e32 v93, 16, v83
	v_and_b32_e32 v83, 0xffff0000, v83
	v_lshlrev_b32_e32 v95, 16, v85
	v_and_b32_e32 v85, 0xffff0000, v85
	v_lshlrev_b32_e32 v97, 16, v87
	v_and_b32_e32 v87, 0xffff0000, v87
	v_lshlrev_b32_e32 v99, 16, v89
	v_and_b32_e32 v89, 0xffff0000, v89
	v_cndmask_b32_e32 v91, v91, v6, vcc
	s_cselect_b64 vcc, -1, 0
	s_cmp_eq_u32 s62, 6
	v_med3_f32 v93, v93, s52, v163
	v_med3_f32 v83, v83, s52, v163
	v_med3_f32 v95, v95, s52, v163
	v_med3_f32 v85, v85, s52, v163
	v_med3_f32 v97, v97, s52, v163
	v_med3_f32 v87, v87, s52, v163
	v_med3_f32 v99, v99, s52, v163
	v_med3_f32 v89, v89, s52, v163
	v_cndmask_b32_e32 v91, v91, v5, vcc
	s_cselect_b64 vcc, -1, 0
	s_cmp_eq_u32 s62, 7
	v_cvt_pk_fp8_f32 v78, v93, v83 op_sel:[0,0,1]
	v_cvt_pk_fp8_f32 v79, v95, v85 op_sel:[0,0,1]
	v_cvt_pk_fp8_f32 v80, v97, v87 op_sel:[0,0,1]
	v_cvt_pk_fp8_f32 v81, v99, v89 op_sel:[0,0,1]
	v_cndmask_b32_e32 v91, v91, v8, vcc
	s_cselect_b64 vcc, -1, 0
	s_add_i32 s2, s2, 2
	s_cmp_eq_u32 s2, 8
	v_cndmask_b32_e32 v91, v91, v7, vcc
	global_store_dwordx4 v90, v[74:77], s[6:7]
	global_store_dwordx4 v91, v[78:81], s[6:7]
	s_cbranch_scc0 .LBB0_289
	s_sleep 55
	s_waitcnt lgkmcnt(0)
	s_add_i32 s61, s61, 1
	s_cmp_eq_u32 s61, 32
	s_cbranch_scc0 .LBB0_286
	s_branch .LBB0_275
